# P11 final-output stores carry the nt (streaming) cache hint; otherwise identical to v86
# baseline (speedup 1.0000x reference)
.LBB0_1339:
	s_add_i32 s1, s8, s2
	s_waitcnt vmcnt(4)
	v_cvt_pk_f32_fp8_e32 v[154:155], v74
	v_cvt_pk_f32_fp8_sdwa v[164:165], v70 src0_sel:WORD_1
	s_cmpk_lt_i32 s1, 0x2000
	v_cvt_pk_f32_fp8_sdwa v[156:157], v74 src0_sel:WORD_1
	v_cvt_pk_f32_fp8_e32 v[158:159], v75
	v_cvt_pk_f32_fp8_sdwa v[160:161], v75 src0_sel:WORD_1
	v_cvt_pk_f32_fp8_e32 v[162:163], v70
	v_cvt_pk_f32_fp8_e32 v[166:167], v71
	v_cvt_pk_f32_fp8_sdwa v[168:169], v71 src0_sel:WORD_1
	v_cvt_pk_f32_fp8_sdwa v[182:183], v69 src0_sel:WORD_1
	v_cvt_pk_f32_fp8_e32 v[184:185], v66
	v_cvt_pk_f32_fp8_sdwa v[194:195], v66 src0_sel:WORD_1
	v_cvt_pk_f32_fp8_e32 v[196:197], v67
	v_cvt_pk_f32_fp8_sdwa v[198:199], v67 src0_sel:WORD_1
	v_cvt_pk_f32_fp8_e32 v[66:67], v72
	v_cvt_pk_f32_fp8_sdwa v[76:77], v80 src0_sel:WORD_1
	s_cselect_b64 s[16:17], -1, 0
	v_cvt_pk_f32_fp8_e32 v[172:173], v68
	v_cvt_pk_f32_fp8_sdwa v[174:175], v68 src0_sel:WORD_1
	v_cvt_pk_f32_fp8_e32 v[180:181], v69
	v_cvt_pk_f32_fp8_sdwa v[68:69], v72 src0_sel:WORD_1
	v_cvt_pk_f32_fp8_e32 v[70:71], v73
	v_cvt_pk_f32_fp8_sdwa v[72:73], v73 src0_sel:WORD_1
	v_cvt_pk_f32_fp8_e32 v[74:75], v80
	v_cvt_pk_f32_fp8_e32 v[78:79], v81
	v_cvt_pk_f32_fp8_sdwa v[80:81], v81 src0_sel:WORD_1
	v_cvt_pk_f32_fp8_e32 v[84:85], v90
	v_cvt_pk_f32_fp8_sdwa v[86:87], v90 src0_sel:WORD_1
	v_cvt_pk_f32_fp8_e32 v[88:89], v91
	v_cvt_pk_f32_fp8_sdwa v[90:91], v91 src0_sel:WORD_1
	v_cvt_pk_f32_fp8_e32 v[92:93], v94
	v_cvt_pk_f32_fp8_sdwa v[148:149], v94 src0_sel:WORD_1
	v_cvt_pk_f32_fp8_e32 v[150:151], v95
	v_cvt_pk_f32_fp8_sdwa v[152:153], v95 src0_sel:WORD_1
	s_waitcnt vmcnt(0)
	v_cvt_pk_f32_fp8_e32 v[94:95], v100
	v_cvt_pk_f32_fp8_sdwa v[104:105], v108 src0_sel:WORD_1
	s_and_b64 vcc, s[16:17], exec
	v_cvt_pk_f32_fp8_sdwa v[96:97], v100 src0_sel:WORD_1
	v_cvt_pk_f32_fp8_e32 v[98:99], v101
	v_cvt_pk_f32_fp8_sdwa v[100:101], v101 src0_sel:WORD_1
	v_cvt_pk_f32_fp8_e32 v[102:103], v108
	v_cvt_pk_f32_fp8_e32 v[106:107], v109
	v_cvt_pk_f32_fp8_sdwa v[108:109], v109 src0_sel:WORD_1
	v_cvt_pk_f32_fp8_e32 v[110:111], v116
	v_cvt_pk_f32_fp8_sdwa v[112:113], v116 src0_sel:WORD_1
	v_cvt_pk_f32_fp8_e32 v[114:115], v117
	v_cvt_pk_f32_fp8_sdwa v[116:117], v117 src0_sel:WORD_1
	v_cvt_pk_f32_fp8_e32 v[118:119], v120
	v_cvt_pk_f32_fp8_sdwa v[170:171], v120 src0_sel:WORD_1
	v_cvt_pk_f32_fp8_e32 v[176:177], v121
	v_cvt_pk_f32_fp8_sdwa v[178:179], v121 src0_sel:WORD_1
	v_cvt_pk_f32_fp8_e32 v[120:121], v126
	v_cvt_pk_f32_fp8_sdwa v[130:131], v134 src0_sel:WORD_1
	s_cselect_b32 s0, s1, s8
	v_cvt_pk_f32_fp8_sdwa v[122:123], v126 src0_sel:WORD_1
	v_cvt_pk_f32_fp8_e32 v[124:125], v127
	v_cvt_pk_f32_fp8_sdwa v[126:127], v127 src0_sel:WORD_1
	v_cvt_pk_f32_fp8_e32 v[128:129], v134
	v_cvt_pk_f32_fp8_e32 v[132:133], v135
	v_cvt_pk_f32_fp8_sdwa v[134:135], v135 src0_sel:WORD_1
	v_cvt_pk_f32_fp8_e32 v[136:137], v142
	v_cvt_pk_f32_fp8_sdwa v[138:139], v142 src0_sel:WORD_1
	v_cvt_pk_f32_fp8_e32 v[140:141], v143
	v_cvt_pk_f32_fp8_sdwa v[142:143], v143 src0_sel:WORD_1
	v_cvt_pk_f32_fp8_sdwa v[186:187], v190 src0_sel:WORD_1
	v_pk_add_f32 v[154:155], v[154:155], 0 op_sel_hi:[1,0]
	v_pk_add_f32 v[164:165], v[164:165], 0 op_sel_hi:[1,0]
	s_mov_b32 s8, s1
	s_ashr_i32 s1, s0, 31
	v_cvt_pk_f32_fp8_e32 v[144:145], v190
	v_cvt_pk_f32_fp8_e32 v[188:189], v191
	v_cvt_pk_f32_fp8_sdwa v[190:191], v191 src0_sel:WORD_1
	v_pk_add_f32 v[194:195], v[194:195], 0 op_sel_hi:[1,0]
	v_pk_add_f32 v[156:157], v[156:157], 0 op_sel_hi:[1,0]
	v_pk_add_f32 v[158:159], v[158:159], 0 op_sel_hi:[1,0]
	v_pk_add_f32 v[160:161], v[160:161], 0 op_sel_hi:[1,0]
	v_pk_add_f32 v[162:163], v[162:163], 0 op_sel_hi:[1,0]
	v_pk_add_f32 v[166:167], v[166:167], 0 op_sel_hi:[1,0]
	v_pk_add_f32 v[168:169], v[168:169], 0 op_sel_hi:[1,0]
	v_pk_add_f32 v[182:183], v[182:183], 0 op_sel_hi:[1,0]
	v_pk_add_f32 v[66:67], v[154:155], v[66:67]
	v_pk_add_f32 v[76:77], v[164:165], v[76:77]
	s_lshl_b64 s[16:17], s[0:1], 13
	v_pk_add_f32 v[198:199], v[198:199], 0 op_sel_hi:[1,0]
	v_pk_add_f32 v[172:173], v[172:173], 0 op_sel_hi:[1,0]
	v_pk_add_f32 v[180:181], v[180:181], 0 op_sel_hi:[1,0]
	v_pk_add_f32 v[184:185], v[184:185], 0 op_sel_hi:[1,0]
	v_pk_add_f32 v[148:149], v[194:195], v[148:149]
	v_pk_add_f32 v[68:69], v[156:157], v[68:69]
	v_pk_add_f32 v[70:71], v[158:159], v[70:71]
	v_pk_add_f32 v[72:73], v[160:161], v[72:73]
	v_pk_add_f32 v[74:75], v[162:163], v[74:75]
	v_pk_add_f32 v[78:79], v[166:167], v[78:79]
	v_pk_add_f32 v[80:81], v[168:169], v[80:81]
	v_pk_add_f32 v[90:91], v[182:183], v[90:91]
	v_pk_add_f32 v[66:67], v[66:67], v[94:95]
	v_pk_add_f32 v[76:77], v[76:77], v[104:105]
	s_add_u32 s16, s13, s16
	v_pk_add_f32 v[196:197], v[196:197], 0 op_sel_hi:[1,0]
	v_pk_add_f32 v[174:175], v[174:175], 0 op_sel_hi:[1,0]
	v_pk_add_f32 v[152:153], v[198:199], v[152:153]
	v_pk_add_f32 v[84:85], v[172:173], v[84:85]
	v_pk_add_f32 v[88:89], v[180:181], v[88:89]
	v_pk_add_f32 v[92:93], v[184:185], v[92:93]
	v_pk_add_f32 v[148:149], v[148:149], v[170:171]
	v_pk_add_f32 v[68:69], v[68:69], v[96:97]
	v_pk_add_f32 v[70:71], v[70:71], v[98:99]
	v_pk_add_f32 v[72:73], v[72:73], v[100:101]
	v_pk_add_f32 v[74:75], v[74:75], v[102:103]
	v_pk_add_f32 v[78:79], v[78:79], v[106:107]
	v_pk_add_f32 v[80:81], v[80:81], v[108:109]
	v_pk_add_f32 v[90:91], v[90:91], v[116:117]
	v_pk_add_f32 v[66:67], v[66:67], v[120:121]
	v_pk_add_f32 v[76:77], v[76:77], v[130:131]
	s_addc_u32 s17, s14, s17
	v_pk_add_f32 v[150:151], v[196:197], v[150:151]
	v_pk_add_f32 v[86:87], v[174:175], v[86:87]
	v_pk_add_f32 v[152:153], v[152:153], v[178:179]
	v_pk_add_f32 v[84:85], v[84:85], v[110:111]
	v_pk_add_f32 v[88:89], v[88:89], v[114:115]
	v_pk_add_f32 v[92:93], v[92:93], v[118:119]
	v_pk_add_f32 v[94:95], v[148:149], v[186:187]
	v_pk_add_f32 v[68:69], v[68:69], v[122:123]
	v_pk_add_f32 v[70:71], v[70:71], v[124:125]
	v_pk_add_f32 v[72:73], v[72:73], v[126:127]
	v_pk_add_f32 v[74:75], v[74:75], v[128:129]
	v_pk_add_f32 v[78:79], v[78:79], v[132:133]
	v_pk_add_f32 v[80:81], v[80:81], v[134:135]
	v_pk_add_f32 v[90:91], v[90:91], v[142:143]
	v_pk_mul_f32 v[114:115], v[66:67], s[12:13] op_sel_hi:[1,0]
	v_pk_mul_f32 v[130:131], v[76:77], s[12:13] op_sel_hi:[1,0]
	v_lshl_add_u64 v[76:77], s[16:17], 0, v[16:17]
	s_add_u32 s18, s16, 0x1000
	v_pk_add_f32 v[150:151], v[150:151], v[176:177]
	v_pk_add_f32 v[86:87], v[86:87], v[112:113]
	v_pk_add_f32 v[98:99], v[152:153], v[190:191]
	v_pk_add_f32 v[84:85], v[84:85], v[136:137]
	v_pk_add_f32 v[92:93], v[92:93], v[144:145]
	v_pk_mul_f32 v[106:107], v[94:95], s[12:13] op_sel_hi:[1,0]
	v_pk_mul_f32 v[118:119], v[68:69], s[12:13] op_sel_hi:[1,0]
	v_pk_mul_f32 v[122:123], v[70:71], s[12:13] op_sel_hi:[1,0]
	v_pk_mul_f32 v[124:125], v[72:73], s[12:13] op_sel_hi:[1,0]
	v_pk_mul_f32 v[128:129], v[74:75], s[12:13] op_sel_hi:[1,0]
	v_pk_mul_f32 v[132:133], v[78:79], s[12:13] op_sel_hi:[1,0]
	v_pk_mul_f32 v[136:137], v[80:81], s[12:13] op_sel_hi:[1,0]
	v_pk_mul_f32 v[144:145], v[90:91], s[12:13] op_sel_hi:[1,0]
	v_pk_mul_f32 v[78:79], v[114:115], v[114:115]
	global_load_dwordx2 v[74:75], v[76:77], off
	global_load_dwordx2 v[70:71], v[76:77], off offset:512
	global_load_dwordx2 v[68:69], v[76:77], off offset:1024
	global_load_dwordx2 v[66:67], v[76:77], off offset:1536
	global_load_dwordx2 v[72:73], v[76:77], off offset:2048
	global_load_dwordx2 v[80:81], v[76:77], off offset:2560
	global_load_dwordx2 v[90:91], v[76:77], off offset:3072
	global_load_dwordx2 v[94:95], v[76:77], off offset:3584
	s_addc_u32 s19, s17, 0
	v_pk_add_f32 v[96:97], v[150:151], v[188:189]
	v_pk_add_f32 v[86:87], v[86:87], v[138:139]
	v_pk_mul_f32 v[112:113], v[98:99], s[12:13] op_sel_hi:[1,0]
	v_pk_mul_f32 v[138:139], v[84:85], s[12:13] op_sel_hi:[1,0]
	v_pk_mul_f32 v[84:85], v[118:119], v[118:119]
	v_add_f32_e32 v98, v78, v79
	s_add_u32 s16, s16, 0x1800
	v_pk_add_f32 v[88:89], v[88:89], v[140:141]
	v_pk_mul_f32 v[110:111], v[96:97], s[12:13] op_sel_hi:[1,0]
	v_pk_mul_f32 v[140:141], v[86:87], s[12:13] op_sel_hi:[1,0]
	v_lshl_add_u64 v[76:77], s[18:19], 0, v[16:17]
	v_lshl_add_u64 v[78:79], s[18:19], 0, v[20:21]
	v_lshl_add_u64 v[86:87], s[18:19], 0, v[22:23]
	v_lshl_add_u64 v[96:97], s[18:19], 0, v[24:25]
	v_add_f32_e32 v84, v98, v84
	s_addc_u32 s17, s17, 0
	s_lshl_b64 s[0:1], s[0:1], 12
	v_pk_mul_f32 v[154:155], v[122:123], v[122:123]
	global_load_dwordx2 v[100:101], v[76:77], off
	global_load_dwordx2 v[108:109], v[78:79], off
	global_load_dwordx2 v[116:117], v[86:87], off
	global_load_dwordx2 v[120:121], v[96:97], off
	v_add_f32_e32 v96, v85, v84
	v_lshl_add_u64 v[76:77], s[16:17], 0, v[16:17]
	v_lshl_add_u64 v[78:79], s[16:17], 0, v[20:21]
	v_lshl_add_u64 v[84:85], s[16:17], 0, v[22:23]
	v_lshl_add_u64 v[86:87], s[16:17], 0, v[24:25]
	v_lshl_add_u64 v[102:103], v[26:27], 0, s[0:1]
	v_add_f32_e32 v154, v154, v96
	global_load_dwordx2 v[126:127], v[76:77], off
	global_load_dwordx2 v[134:135], v[78:79], off
	global_load_dwordx2 v[142:143], v[84:85], off
	global_load_dwordx2 v[190:191], v[86:87], off
	s_nop 0
	global_load_dwordx4 v[76:79], v[102:103], off
	global_load_dwordx4 v[84:87], v[102:103], off offset:1024
	global_load_dwordx4 v[96:99], v[102:103], off offset:2048
	s_nop 0
	global_load_dwordx4 v[102:105], v[102:103], off offset:3072
	v_pk_mul_f32 v[156:157], v[124:125], v[124:125]
	v_add_f32_e32 v154, v155, v154
	v_add_f32_e32 v154, v156, v154
	v_pk_mul_f32 v[158:159], v[128:129], v[128:129]
	v_add_f32_e32 v154, v157, v154
	v_add_f32_e32 v154, v158, v154
	v_pk_mul_f32 v[160:161], v[130:131], v[130:131]
	v_add_f32_e32 v154, v159, v154
	v_add_f32_e32 v154, v160, v154
	v_pk_mul_f32 v[162:163], v[132:133], v[132:133]
	v_add_f32_e32 v154, v161, v154
	v_add_f32_e32 v154, v162, v154
	v_pk_mul_f32 v[164:165], v[136:137], v[136:137]
	v_add_f32_e32 v154, v163, v154
	v_add_f32_e32 v154, v164, v154
	v_pk_mul_f32 v[166:167], v[138:139], v[138:139]
	v_add_f32_e32 v154, v165, v154
	v_add_f32_e32 v154, v166, v154
	v_pk_mul_f32 v[168:169], v[140:141], v[140:141]
	v_add_f32_e32 v154, v167, v154
	v_pk_mul_f32 v[88:89], v[88:89], s[12:13] op_sel_hi:[1,0]
	v_add_f32_e32 v154, v168, v154
	v_pk_mul_f32 v[170:171], v[88:89], v[88:89]
	v_add_f32_e32 v154, v169, v154
	v_add_f32_e32 v154, v170, v154
	v_pk_mul_f32 v[172:173], v[144:145], v[144:145]
	v_add_f32_e32 v154, v171, v154
	v_pk_mul_f32 v[92:93], v[92:93], s[12:13] op_sel_hi:[1,0]
	v_add_f32_e32 v154, v172, v154
	v_pk_mul_f32 v[174:175], v[92:93], v[92:93]
	v_add_f32_e32 v154, v173, v154
	v_add_f32_e32 v154, v174, v154
	v_pk_mul_f32 v[148:149], v[106:107], v[106:107]
	v_add_f32_e32 v154, v175, v154
	v_add_f32_e32 v148, v148, v154
	v_pk_mul_f32 v[150:151], v[110:111], v[110:111]
	v_add_f32_e32 v148, v149, v148
	v_add_f32_e32 v148, v150, v148
	v_pk_mul_f32 v[152:153], v[112:113], v[112:113]
	v_add_f32_e32 v148, v151, v148
	v_add_f32_e32 v148, v152, v148
	v_add_f32_e32 v148, v153, v148
	v_lshlrev_b32_e32 v62, 16, v12
	v_and_b32_e32 v63, 0xffff0000, v12
	v_add_f32_dpp v148, v148, v148 quad_perm:[1,0,3,2] row_mask:0xf bank_mask:0xf bound_ctrl:1
	v_lshlrev_b32_e32 v12, 16, v13
	v_and_b32_e32 v13, 0xffff0000, v13
	v_add_f32_dpp v148, v148, v148 quad_perm:[2,3,0,1] row_mask:0xf bank_mask:0xf bound_ctrl:1
	v_lshlrev_b32_e32 v64, 16, v14
	v_and_b32_e32 v65, 0xffff0000, v14
	v_add_f32_dpp v148, v148, v148 row_ror:4 row_mask:0xf bank_mask:0xf bound_ctrl:1
	v_lshlrev_b32_e32 v14, 16, v15
	v_and_b32_e32 v15, 0xffff0000, v15
	v_add_f32_dpp v148, v148, v148 row_ror:8 row_mask:0xf bank_mask:0xf bound_ctrl:1
	v_lshlrev_b32_e32 v82, 16, v8
	v_readlane_b32 s9, v148, 16
	v_readlane_b32 s15, v148, 48
	v_readlane_b32 s0, v148, 0
	v_readlane_b32 s1, v148, 32
	v_mov_b32_e32 v148, s9
	v_mov_b32_e32 v149, s15
	v_pk_add_f32 v[148:149], s[0:1], v[148:149]
	v_and_b32_e32 v83, 0xffff0000, v8
	v_add_f32_e32 v148, v148, v149
	v_fmamk_f32 v148, v148, 0x3a000000, v19
	v_mul_f32_e32 v149, 0x4b800000, v148
	v_cmp_gt_f32_e64 s[0:1], s3, v148
	v_lshlrev_b32_e32 v8, 16, v9
	v_and_b32_e32 v9, 0xffff0000, v9
	v_cndmask_b32_e64 v148, v148, v149, s[0:1]
	v_rsq_f32_e32 v148, v148
	v_lshlrev_b32_e32 v146, 16, v10
	v_and_b32_e32 v147, 0xffff0000, v10
	v_lshlrev_b32_e32 v10, 16, v11
	v_mul_f32_e32 v149, 0x45800000, v148
	v_cndmask_b32_e64 v148, v148, v149, s[0:1]
	v_and_b32_e32 v11, 0xffff0000, v11
	v_lshlrev_b32_e32 v192, 16, v4
	v_and_b32_e32 v193, 0xffff0000, v4
	v_lshlrev_b32_e32 v4, 16, v5
	v_and_b32_e32 v5, 0xffff0000, v5
	v_lshlrev_b32_e32 v200, 16, v6
	v_and_b32_e32 v201, 0xffff0000, v6
	v_lshlrev_b32_e32 v6, 16, v7
	v_and_b32_e32 v7, 0xffff0000, v7
	v_lshlrev_b32_e32 v202, 16, v0
	v_and_b32_e32 v203, 0xffff0000, v0
	v_lshlrev_b32_e32 v0, 16, v1
	v_and_b32_e32 v1, 0xffff0000, v1
	v_lshlrev_b32_e32 v204, 16, v2
	v_and_b32_e32 v205, 0xffff0000, v2
	v_lshlrev_b32_e32 v2, 16, v3
	v_and_b32_e32 v3, 0xffff0000, v3
	v_pk_mul_f32 v[114:115], v[114:115], v[148:149] op_sel_hi:[1,0]
	v_pk_mul_f32 v[118:119], v[118:119], v[148:149] op_sel_hi:[1,0]
	v_pk_mul_f32 v[122:123], v[122:123], v[148:149] op_sel_hi:[1,0]
	v_pk_mul_f32 v[124:125], v[124:125], v[148:149] op_sel_hi:[1,0]
	v_pk_mul_f32 v[128:129], v[128:129], v[148:149] op_sel_hi:[1,0]
	v_pk_mul_f32 v[130:131], v[130:131], v[148:149] op_sel_hi:[1,0]
	v_pk_mul_f32 v[132:133], v[132:133], v[148:149] op_sel_hi:[1,0]
	v_pk_mul_f32 v[136:137], v[136:137], v[148:149] op_sel_hi:[1,0]
	v_pk_mul_f32 v[138:139], v[138:139], v[148:149] op_sel_hi:[1,0]
	v_pk_mul_f32 v[140:141], v[140:141], v[148:149] op_sel_hi:[1,0]
	v_pk_mul_f32 v[88:89], v[88:89], v[148:149] op_sel_hi:[1,0]
	v_pk_mul_f32 v[144:145], v[144:145], v[148:149] op_sel_hi:[1,0]
	v_pk_mul_f32 v[92:93], v[92:93], v[148:149] op_sel_hi:[1,0]
	v_pk_mul_f32 v[106:107], v[106:107], v[148:149] op_sel_hi:[1,0]
	v_pk_mul_f32 v[150:151], v[110:111], v[148:149] op_sel_hi:[1,0]
	v_pk_mul_f32 v[148:149], v[112:113], v[148:149] op_sel_hi:[1,0]
	v_pk_fma_f32 v[110:111], v[30:31], v[114:115], v[62:63]
	v_pk_fma_f32 v[112:113], v[28:29], v[118:119], v[12:13]
	v_pk_fma_f32 v[12:13], v[34:35], v[122:123], v[64:65]
	v_pk_fma_f32 v[14:15], v[32:33], v[124:125], v[14:15]
	v_pk_fma_f32 v[64:65], v[36:37], v[130:131], v[8:9]
	v_pk_fma_f32 v[8:9], v[42:43], v[132:133], v[146:147]
	v_pk_fma_f32 v[10:11], v[40:41], v[136:137], v[10:11]
	v_pk_fma_f32 v[124:125], v[44:45], v[140:141], v[4:5]
	v_pk_fma_f32 v[4:5], v[50:51], v[88:89], v[200:201]
	v_pk_fma_f32 v[6:7], v[48:49], v[144:145], v[6:7]
	v_pk_fma_f32 v[130:131], v[52:53], v[106:107], v[0:1]
	v_pk_fma_f32 v[0:1], v[58:59], v[150:151], v[204:205]
	v_pk_fma_f32 v[2:3], v[56:57], v[148:149], v[2:3]
	v_pk_fma_f32 v[62:63], v[38:39], v[128:129], v[82:83]
	v_pk_fma_f32 v[122:123], v[46:47], v[138:139], v[192:193]
	v_pk_fma_f32 v[128:129], v[54:55], v[92:93], v[202:203]
	global_store_dwordx4 v[60:61], v[110:113], off offset:-4096 nt
	global_store_dwordx4 v[60:61], v[12:15], off offset:-4080 nt
	global_store_dwordx4 v[60:61], v[62:65], off offset:-2048 nt
	global_store_dwordx4 v[60:61], v[8:11], off offset:-2032 nt
	global_store_dwordx4 v[60:61], v[122:125], off nt
	global_store_dwordx4 v[60:61], v[4:7], off offset:16 nt
	global_store_dwordx4 v[60:61], v[128:131], off offset:2048 nt
	global_store_dwordx4 v[60:61], v[0:3], off offset:2064 nt
	s_waitcnt vmcnt(9)
	v_mov_b64_e32 v[4:5], v[96:97]
	v_mov_b64_e32 v[8:9], v[84:85]
	s_waitcnt vmcnt(8)
	v_mov_b64_e32 v[0:1], v[102:103]
	v_mov_b64_e32 v[12:13], v[76:77]
	v_lshl_add_u64 v[60:61], v[60:61], 0, s[10:11]
	v_mov_b64_e32 v[2:3], v[104:105]
	v_mov_b64_e32 v[6:7], v[98:99]
	v_mov_b64_e32 v[10:11], v[86:87]
	v_mov_b64_e32 v[14:15], v[78:79]
	s_cbranch_vccnz .LBB0_1339

.LBB0_1344:
	s_add_i32 s1, s4, s2
	s_waitcnt vmcnt(0)
	v_cvt_pk_f32_fp8_e32 v[152:153], v72
	v_cvt_pk_f32_fp8_sdwa v[162:163], v68 src0_sel:WORD_1
	s_cmpk_lt_i32 s1, 0x4000
	v_cvt_pk_f32_fp8_sdwa v[154:155], v72 src0_sel:WORD_1
	v_cvt_pk_f32_fp8_e32 v[156:157], v73
	v_cvt_pk_f32_fp8_sdwa v[158:159], v73 src0_sel:WORD_1
	v_cvt_pk_f32_fp8_e32 v[160:161], v68
	v_cvt_pk_f32_fp8_e32 v[164:165], v69
	v_cvt_pk_f32_fp8_sdwa v[166:167], v69 src0_sel:WORD_1
	v_cvt_pk_f32_fp8_sdwa v[180:181], v67 src0_sel:WORD_1
	v_cvt_pk_f32_fp8_e32 v[182:183], v64
	v_cvt_pk_f32_fp8_sdwa v[192:193], v64 src0_sel:WORD_1
	v_cvt_pk_f32_fp8_e32 v[194:195], v65
	v_cvt_pk_f32_fp8_sdwa v[196:197], v65 src0_sel:WORD_1
	v_cvt_pk_f32_fp8_e32 v[64:65], v70
	v_cvt_pk_f32_fp8_sdwa v[74:75], v78 src0_sel:WORD_1
	s_cselect_b64 s[10:11], -1, 0
	v_cvt_pk_f32_fp8_e32 v[170:171], v66
	v_cvt_pk_f32_fp8_sdwa v[172:173], v66 src0_sel:WORD_1
	v_cvt_pk_f32_fp8_e32 v[178:179], v67
	v_cvt_pk_f32_fp8_sdwa v[66:67], v70 src0_sel:WORD_1
	v_cvt_pk_f32_fp8_e32 v[68:69], v71
	v_cvt_pk_f32_fp8_sdwa v[70:71], v71 src0_sel:WORD_1
	v_cvt_pk_f32_fp8_e32 v[72:73], v78
	v_cvt_pk_f32_fp8_e32 v[76:77], v79
	v_cvt_pk_f32_fp8_sdwa v[78:79], v79 src0_sel:WORD_1
	v_cvt_pk_f32_fp8_e32 v[82:83], v88
	v_cvt_pk_f32_fp8_sdwa v[84:85], v88 src0_sel:WORD_1
	v_cvt_pk_f32_fp8_e32 v[86:87], v89
	v_cvt_pk_f32_fp8_sdwa v[88:89], v89 src0_sel:WORD_1
	v_cvt_pk_f32_fp8_e32 v[90:91], v92
	v_cvt_pk_f32_fp8_sdwa v[146:147], v92 src0_sel:WORD_1
	v_cvt_pk_f32_fp8_e32 v[148:149], v93
	v_cvt_pk_f32_fp8_sdwa v[150:151], v93 src0_sel:WORD_1
	v_cvt_pk_f32_fp8_e32 v[92:93], v98
	v_cvt_pk_f32_fp8_sdwa v[102:103], v106 src0_sel:WORD_1
	s_and_b64 vcc, s[10:11], exec
	v_cvt_pk_f32_fp8_sdwa v[94:95], v98 src0_sel:WORD_1
	v_cvt_pk_f32_fp8_e32 v[96:97], v99
	v_cvt_pk_f32_fp8_sdwa v[98:99], v99 src0_sel:WORD_1
	v_cvt_pk_f32_fp8_e32 v[100:101], v106
	v_cvt_pk_f32_fp8_e32 v[104:105], v107
	v_cvt_pk_f32_fp8_sdwa v[106:107], v107 src0_sel:WORD_1
	v_cvt_pk_f32_fp8_e32 v[108:109], v114
	v_cvt_pk_f32_fp8_sdwa v[110:111], v114 src0_sel:WORD_1
	v_cvt_pk_f32_fp8_e32 v[112:113], v115
	v_cvt_pk_f32_fp8_sdwa v[114:115], v115 src0_sel:WORD_1
	v_cvt_pk_f32_fp8_e32 v[116:117], v118
	v_cvt_pk_f32_fp8_sdwa v[168:169], v118 src0_sel:WORD_1
	v_cvt_pk_f32_fp8_e32 v[174:175], v119
	v_cvt_pk_f32_fp8_sdwa v[176:177], v119 src0_sel:WORD_1
	v_cvt_pk_f32_fp8_e32 v[118:119], v124
	v_cvt_pk_f32_fp8_sdwa v[128:129], v132 src0_sel:WORD_1
	s_cselect_b32 s0, s1, s4
	v_cvt_pk_f32_fp8_sdwa v[120:121], v124 src0_sel:WORD_1
	v_cvt_pk_f32_fp8_e32 v[122:123], v125
	v_cvt_pk_f32_fp8_sdwa v[124:125], v125 src0_sel:WORD_1
	v_cvt_pk_f32_fp8_e32 v[126:127], v132
	v_cvt_pk_f32_fp8_e32 v[130:131], v133
	v_cvt_pk_f32_fp8_sdwa v[132:133], v133 src0_sel:WORD_1
	v_cvt_pk_f32_fp8_e32 v[134:135], v140
	v_cvt_pk_f32_fp8_sdwa v[136:137], v140 src0_sel:WORD_1
	v_cvt_pk_f32_fp8_e32 v[138:139], v141
	v_cvt_pk_f32_fp8_sdwa v[140:141], v141 src0_sel:WORD_1
	v_cvt_pk_f32_fp8_sdwa v[184:185], v188 src0_sel:WORD_1
	v_pk_add_f32 v[152:153], v[152:153], 0 op_sel_hi:[1,0]
	v_pk_add_f32 v[162:163], v[162:163], 0 op_sel_hi:[1,0]
	s_mov_b32 s4, s1
	s_ashr_i32 s1, s0, 31
	v_cvt_pk_f32_fp8_e32 v[142:143], v188
	v_cvt_pk_f32_fp8_e32 v[186:187], v189
	v_cvt_pk_f32_fp8_sdwa v[188:189], v189 src0_sel:WORD_1
	v_pk_add_f32 v[192:193], v[192:193], 0 op_sel_hi:[1,0]
	v_pk_add_f32 v[154:155], v[154:155], 0 op_sel_hi:[1,0]
	v_pk_add_f32 v[156:157], v[156:157], 0 op_sel_hi:[1,0]
	v_pk_add_f32 v[158:159], v[158:159], 0 op_sel_hi:[1,0]
	v_pk_add_f32 v[160:161], v[160:161], 0 op_sel_hi:[1,0]
	v_pk_add_f32 v[164:165], v[164:165], 0 op_sel_hi:[1,0]
	v_pk_add_f32 v[166:167], v[166:167], 0 op_sel_hi:[1,0]
	v_pk_add_f32 v[180:181], v[180:181], 0 op_sel_hi:[1,0]
	v_pk_add_f32 v[64:65], v[152:153], v[64:65]
	v_pk_add_f32 v[74:75], v[162:163], v[74:75]
	s_lshl_b64 s[10:11], s[0:1], 13
	v_pk_add_f32 v[196:197], v[196:197], 0 op_sel_hi:[1,0]
	v_pk_add_f32 v[170:171], v[170:171], 0 op_sel_hi:[1,0]
	v_pk_add_f32 v[178:179], v[178:179], 0 op_sel_hi:[1,0]
	v_pk_add_f32 v[182:183], v[182:183], 0 op_sel_hi:[1,0]
	v_pk_add_f32 v[146:147], v[192:193], v[146:147]
	v_pk_add_f32 v[66:67], v[154:155], v[66:67]
	v_pk_add_f32 v[68:69], v[156:157], v[68:69]
	v_pk_add_f32 v[70:71], v[158:159], v[70:71]
	v_pk_add_f32 v[72:73], v[160:161], v[72:73]
	v_pk_add_f32 v[76:77], v[164:165], v[76:77]
	v_pk_add_f32 v[78:79], v[166:167], v[78:79]
	v_pk_add_f32 v[88:89], v[180:181], v[88:89]
	v_pk_add_f32 v[64:65], v[64:65], v[92:93]
	v_pk_add_f32 v[74:75], v[74:75], v[102:103]
	s_add_u32 s10, s13, s10
	v_pk_add_f32 v[194:195], v[194:195], 0 op_sel_hi:[1,0]
	v_pk_add_f32 v[172:173], v[172:173], 0 op_sel_hi:[1,0]
	v_pk_add_f32 v[150:151], v[196:197], v[150:151]
	v_pk_add_f32 v[82:83], v[170:171], v[82:83]
	v_pk_add_f32 v[86:87], v[178:179], v[86:87]
	v_pk_add_f32 v[90:91], v[182:183], v[90:91]
	v_pk_add_f32 v[146:147], v[146:147], v[168:169]
	v_pk_add_f32 v[66:67], v[66:67], v[94:95]
	v_pk_add_f32 v[68:69], v[68:69], v[96:97]
	v_pk_add_f32 v[70:71], v[70:71], v[98:99]
	v_pk_add_f32 v[72:73], v[72:73], v[100:101]
	v_pk_add_f32 v[76:77], v[76:77], v[104:105]
	v_pk_add_f32 v[78:79], v[78:79], v[106:107]
	v_pk_add_f32 v[88:89], v[88:89], v[114:115]
	v_pk_add_f32 v[64:65], v[64:65], v[118:119]
	v_pk_add_f32 v[74:75], v[74:75], v[128:129]
	s_addc_u32 s11, s14, s11
	v_pk_add_f32 v[148:149], v[194:195], v[148:149]
	v_pk_add_f32 v[84:85], v[172:173], v[84:85]
	v_pk_add_f32 v[150:151], v[150:151], v[176:177]
	v_pk_add_f32 v[82:83], v[82:83], v[108:109]
	v_pk_add_f32 v[86:87], v[86:87], v[112:113]
	v_pk_add_f32 v[90:91], v[90:91], v[116:117]
	v_pk_add_f32 v[92:93], v[146:147], v[184:185]
	v_pk_add_f32 v[66:67], v[66:67], v[120:121]
	v_pk_add_f32 v[68:69], v[68:69], v[122:123]
	v_pk_add_f32 v[70:71], v[70:71], v[124:125]
	v_pk_add_f32 v[72:73], v[72:73], v[126:127]
	v_pk_add_f32 v[76:77], v[76:77], v[130:131]
	v_pk_add_f32 v[78:79], v[78:79], v[132:133]
	v_pk_add_f32 v[88:89], v[88:89], v[140:141]
	v_pk_mul_f32 v[112:113], v[64:65], s[8:9] op_sel_hi:[1,0]
	v_pk_mul_f32 v[128:129], v[74:75], s[8:9] op_sel_hi:[1,0]
	v_lshl_add_u64 v[74:75], s[10:11], 0, v[16:17]
	s_add_u32 s16, s10, 0x1000
	v_pk_add_f32 v[148:149], v[148:149], v[174:175]
	v_pk_add_f32 v[84:85], v[84:85], v[110:111]
	v_pk_add_f32 v[96:97], v[150:151], v[188:189]
	v_pk_add_f32 v[82:83], v[82:83], v[134:135]
	v_pk_add_f32 v[90:91], v[90:91], v[142:143]
	v_pk_mul_f32 v[104:105], v[92:93], s[8:9] op_sel_hi:[1,0]
	v_pk_mul_f32 v[116:117], v[66:67], s[8:9] op_sel_hi:[1,0]
	v_pk_mul_f32 v[120:121], v[68:69], s[8:9] op_sel_hi:[1,0]
	v_pk_mul_f32 v[122:123], v[70:71], s[8:9] op_sel_hi:[1,0]
	v_pk_mul_f32 v[126:127], v[72:73], s[8:9] op_sel_hi:[1,0]
	v_pk_mul_f32 v[130:131], v[76:77], s[8:9] op_sel_hi:[1,0]
	v_pk_mul_f32 v[134:135], v[78:79], s[8:9] op_sel_hi:[1,0]
	v_pk_mul_f32 v[142:143], v[88:89], s[8:9] op_sel_hi:[1,0]
	v_pk_mul_f32 v[76:77], v[112:113], v[112:113]
	global_load_dwordx2 v[72:73], v[74:75], off
	global_load_dwordx2 v[68:69], v[74:75], off offset:512
	global_load_dwordx2 v[66:67], v[74:75], off offset:1024
	global_load_dwordx2 v[64:65], v[74:75], off offset:1536
	global_load_dwordx2 v[70:71], v[74:75], off offset:2048
	global_load_dwordx2 v[78:79], v[74:75], off offset:2560
	global_load_dwordx2 v[88:89], v[74:75], off offset:3072
	global_load_dwordx2 v[92:93], v[74:75], off offset:3584
	s_addc_u32 s17, s11, 0
	v_pk_add_f32 v[94:95], v[148:149], v[186:187]
	v_pk_add_f32 v[84:85], v[84:85], v[136:137]
	v_pk_mul_f32 v[110:111], v[96:97], s[8:9] op_sel_hi:[1,0]
	v_pk_mul_f32 v[136:137], v[82:83], s[8:9] op_sel_hi:[1,0]
	v_pk_mul_f32 v[82:83], v[116:117], v[116:117]
	v_add_f32_e32 v96, v76, v77
	s_add_u32 s10, s10, 0x1800
	v_pk_add_f32 v[86:87], v[86:87], v[138:139]
	v_pk_mul_f32 v[108:109], v[94:95], s[8:9] op_sel_hi:[1,0]
	v_pk_mul_f32 v[138:139], v[84:85], s[8:9] op_sel_hi:[1,0]
	v_lshl_add_u64 v[74:75], s[16:17], 0, v[16:17]
	v_lshl_add_u64 v[76:77], s[16:17], 0, v[20:21]
	v_lshl_add_u64 v[84:85], s[16:17], 0, v[22:23]
	v_lshl_add_u64 v[94:95], s[16:17], 0, v[24:25]
	v_add_f32_e32 v82, v96, v82
	s_addc_u32 s11, s11, 0
	s_lshl_b64 s[0:1], s[0:1], 12
	v_pk_mul_f32 v[152:153], v[120:121], v[120:121]
	global_load_dwordx2 v[98:99], v[74:75], off
	global_load_dwordx2 v[106:107], v[76:77], off
	global_load_dwordx2 v[114:115], v[84:85], off
	global_load_dwordx2 v[118:119], v[94:95], off
	v_add_f32_e32 v94, v83, v82
	v_lshl_add_u64 v[74:75], s[10:11], 0, v[16:17]
	v_lshl_add_u64 v[76:77], s[10:11], 0, v[20:21]
	v_lshl_add_u64 v[82:83], s[10:11], 0, v[22:23]
	v_lshl_add_u64 v[84:85], s[10:11], 0, v[24:25]
	v_lshl_add_u64 v[100:101], v[18:19], 0, s[0:1]
	v_add_f32_e32 v152, v152, v94
	global_load_dwordx2 v[124:125], v[74:75], off
	global_load_dwordx2 v[132:133], v[76:77], off
	global_load_dwordx2 v[140:141], v[82:83], off
	global_load_dwordx2 v[188:189], v[84:85], off
	s_nop 0
	global_load_dwordx4 v[74:77], v[100:101], off
	global_load_dwordx4 v[82:85], v[100:101], off offset:1024
	global_load_dwordx4 v[94:97], v[100:101], off offset:2048
	s_nop 0
	global_load_dwordx4 v[100:103], v[100:101], off offset:3072
	v_pk_mul_f32 v[154:155], v[122:123], v[122:123]
	v_add_f32_e32 v152, v153, v152
	v_add_f32_e32 v152, v154, v152
	v_pk_mul_f32 v[156:157], v[126:127], v[126:127]
	v_add_f32_e32 v152, v155, v152
	v_add_f32_e32 v152, v156, v152
	v_pk_mul_f32 v[158:159], v[128:129], v[128:129]
	v_add_f32_e32 v152, v157, v152
	v_add_f32_e32 v152, v158, v152
	v_pk_mul_f32 v[160:161], v[130:131], v[130:131]
	v_add_f32_e32 v152, v159, v152
	v_add_f32_e32 v152, v160, v152
	v_pk_mul_f32 v[162:163], v[134:135], v[134:135]
	v_add_f32_e32 v152, v161, v152
	v_add_f32_e32 v152, v162, v152
	v_pk_mul_f32 v[164:165], v[136:137], v[136:137]
	v_add_f32_e32 v152, v163, v152
	v_add_f32_e32 v152, v164, v152
	v_pk_mul_f32 v[166:167], v[138:139], v[138:139]
	v_add_f32_e32 v152, v165, v152
	v_pk_mul_f32 v[86:87], v[86:87], s[8:9] op_sel_hi:[1,0]
	v_add_f32_e32 v152, v166, v152
	v_pk_mul_f32 v[168:169], v[86:87], v[86:87]
	v_add_f32_e32 v152, v167, v152
	v_add_f32_e32 v152, v168, v152
	v_pk_mul_f32 v[170:171], v[142:143], v[142:143]
	v_add_f32_e32 v152, v169, v152
	v_pk_mul_f32 v[90:91], v[90:91], s[8:9] op_sel_hi:[1,0]
	v_add_f32_e32 v152, v170, v152
	v_pk_mul_f32 v[172:173], v[90:91], v[90:91]
	v_add_f32_e32 v152, v171, v152
	v_add_f32_e32 v152, v172, v152
	v_pk_mul_f32 v[146:147], v[104:105], v[104:105]
	v_add_f32_e32 v152, v173, v152
	v_add_f32_e32 v146, v146, v152
	v_pk_mul_f32 v[148:149], v[108:109], v[108:109]
	v_add_f32_e32 v146, v147, v146
	v_add_f32_e32 v146, v148, v146
	v_pk_mul_f32 v[150:151], v[110:111], v[110:111]
	v_add_f32_e32 v146, v149, v146
	v_add_f32_e32 v146, v150, v146
	v_add_f32_e32 v146, v151, v146
	v_lshlrev_b32_e32 v60, 16, v12
	v_and_b32_e32 v61, 0xffff0000, v12
	v_add_f32_dpp v146, v146, v146 quad_perm:[1,0,3,2] row_mask:0xf bank_mask:0xf bound_ctrl:1
	v_lshlrev_b32_e32 v12, 16, v13
	v_and_b32_e32 v13, 0xffff0000, v13
	v_add_f32_dpp v146, v146, v146 quad_perm:[2,3,0,1] row_mask:0xf bank_mask:0xf bound_ctrl:1
	v_lshlrev_b32_e32 v62, 16, v14
	v_and_b32_e32 v63, 0xffff0000, v14
	v_add_f32_dpp v146, v146, v146 row_ror:4 row_mask:0xf bank_mask:0xf bound_ctrl:1
	v_lshlrev_b32_e32 v14, 16, v15
	v_and_b32_e32 v15, 0xffff0000, v15
	v_add_f32_dpp v146, v146, v146 row_ror:8 row_mask:0xf bank_mask:0xf bound_ctrl:1
	v_lshlrev_b32_e32 v80, 16, v8
	v_readlane_b32 s5, v146, 16
	v_readlane_b32 s9, v146, 48
	v_readlane_b32 s0, v146, 0
	v_readlane_b32 s1, v146, 32
	v_mov_b32_e32 v146, s5
	v_mov_b32_e32 v147, s9
	v_pk_add_f32 v[146:147], s[0:1], v[146:147]
	v_and_b32_e32 v81, 0xffff0000, v8
	v_add_f32_e32 v146, v146, v147
	v_fmamk_f32 v146, v146, 0x3a000000, v204
	v_mul_f32_e32 v147, 0x4b800000, v146
	v_cmp_gt_f32_e64 s[0:1], s3, v146
	v_lshlrev_b32_e32 v8, 16, v9
	v_and_b32_e32 v9, 0xffff0000, v9
	v_cndmask_b32_e64 v146, v146, v147, s[0:1]
	v_rsq_f32_e32 v146, v146
	v_lshlrev_b32_e32 v144, 16, v10
	v_and_b32_e32 v145, 0xffff0000, v10
	v_lshlrev_b32_e32 v10, 16, v11
	v_mul_f32_e32 v147, 0x45800000, v146
	v_cndmask_b32_e64 v146, v146, v147, s[0:1]
	v_and_b32_e32 v11, 0xffff0000, v11
	v_lshlrev_b32_e32 v190, 16, v4
	v_and_b32_e32 v191, 0xffff0000, v4
	v_lshlrev_b32_e32 v4, 16, v5
	v_and_b32_e32 v5, 0xffff0000, v5
	v_lshlrev_b32_e32 v198, 16, v6
	v_and_b32_e32 v199, 0xffff0000, v6
	v_lshlrev_b32_e32 v6, 16, v7
	v_and_b32_e32 v7, 0xffff0000, v7
	v_lshlrev_b32_e32 v200, 16, v0
	v_and_b32_e32 v201, 0xffff0000, v0
	v_lshlrev_b32_e32 v0, 16, v1
	v_and_b32_e32 v1, 0xffff0000, v1
	v_lshlrev_b32_e32 v202, 16, v2
	v_and_b32_e32 v203, 0xffff0000, v2
	v_lshlrev_b32_e32 v2, 16, v3
	v_and_b32_e32 v3, 0xffff0000, v3
	v_pk_mul_f32 v[112:113], v[112:113], v[146:147] op_sel_hi:[1,0]
	v_pk_mul_f32 v[116:117], v[116:117], v[146:147] op_sel_hi:[1,0]
	v_pk_mul_f32 v[120:121], v[120:121], v[146:147] op_sel_hi:[1,0]
	v_pk_mul_f32 v[122:123], v[122:123], v[146:147] op_sel_hi:[1,0]
	v_pk_mul_f32 v[126:127], v[126:127], v[146:147] op_sel_hi:[1,0]
	v_pk_mul_f32 v[128:129], v[128:129], v[146:147] op_sel_hi:[1,0]
	v_pk_mul_f32 v[130:131], v[130:131], v[146:147] op_sel_hi:[1,0]
	v_pk_mul_f32 v[134:135], v[134:135], v[146:147] op_sel_hi:[1,0]
	v_pk_mul_f32 v[136:137], v[136:137], v[146:147] op_sel_hi:[1,0]
	v_pk_mul_f32 v[138:139], v[138:139], v[146:147] op_sel_hi:[1,0]
	v_pk_mul_f32 v[86:87], v[86:87], v[146:147] op_sel_hi:[1,0]
	v_pk_mul_f32 v[142:143], v[142:143], v[146:147] op_sel_hi:[1,0]
	v_pk_mul_f32 v[90:91], v[90:91], v[146:147] op_sel_hi:[1,0]
	v_pk_mul_f32 v[104:105], v[104:105], v[146:147] op_sel_hi:[1,0]
	v_pk_mul_f32 v[148:149], v[108:109], v[146:147] op_sel_hi:[1,0]
	v_pk_mul_f32 v[146:147], v[110:111], v[146:147] op_sel_hi:[1,0]
	v_pk_fma_f32 v[108:109], v[28:29], v[112:113], v[60:61]
	v_pk_fma_f32 v[110:111], v[26:27], v[116:117], v[12:13]
	v_pk_fma_f32 v[12:13], v[32:33], v[120:121], v[62:63]
	v_pk_fma_f32 v[14:15], v[30:31], v[122:123], v[14:15]
	v_pk_fma_f32 v[62:63], v[34:35], v[128:129], v[8:9]
	v_pk_fma_f32 v[8:9], v[40:41], v[130:131], v[144:145]
	v_pk_fma_f32 v[10:11], v[38:39], v[134:135], v[10:11]
	v_pk_fma_f32 v[122:123], v[42:43], v[138:139], v[4:5]
	v_pk_fma_f32 v[4:5], v[48:49], v[86:87], v[198:199]
	v_pk_fma_f32 v[6:7], v[46:47], v[142:143], v[6:7]
	v_pk_fma_f32 v[128:129], v[50:51], v[104:105], v[0:1]
	v_pk_fma_f32 v[0:1], v[56:57], v[148:149], v[202:203]
	v_pk_fma_f32 v[2:3], v[54:55], v[146:147], v[2:3]
	v_pk_fma_f32 v[60:61], v[36:37], v[126:127], v[80:81]
	v_pk_fma_f32 v[120:121], v[44:45], v[136:137], v[190:191]
	v_pk_fma_f32 v[126:127], v[52:53], v[90:91], v[200:201]
	global_store_dwordx4 v[58:59], v[108:111], off offset:-4096 nt
	global_store_dwordx4 v[58:59], v[12:15], off offset:-4080 nt
	global_store_dwordx4 v[58:59], v[60:63], off offset:-2048 nt
	global_store_dwordx4 v[58:59], v[8:11], off offset:-2032 nt
	global_store_dwordx4 v[58:59], v[120:123], off nt
	global_store_dwordx4 v[58:59], v[4:7], off offset:16 nt
	global_store_dwordx4 v[58:59], v[126:129], off offset:2048 nt
	global_store_dwordx4 v[58:59], v[0:3], off offset:2064 nt
	s_waitcnt vmcnt(9)
	v_mov_b64_e32 v[4:5], v[94:95]
	v_mov_b64_e32 v[8:9], v[82:83]
	s_waitcnt vmcnt(8)
	v_mov_b64_e32 v[0:1], v[100:101]
	v_mov_b64_e32 v[12:13], v[74:75]
	v_lshl_add_u64 v[58:59], v[58:59], 0, s[6:7]
	v_mov_b64_e32 v[2:3], v[102:103]
	v_mov_b64_e32 v[6:7], v[96:97]
	v_mov_b64_e32 v[10:11], v[84:85]
	v_mov_b64_e32 v[14:15], v[76:77]
	s_cbranch_vccnz .LBB0_1344
